# grid barrier v2: every workgroup waits on the monotonic cross-XCD arrival counter (no release words, no hop through XCD leaders); without the P1 tile permutation
# baseline (speedup 1.0000x reference)
.LBB0_81:
	s_or_b64 exec, exec, s[10:11]
	v_cvt_f32_u32_e32 v5, v3
	s_waitcnt vmcnt(0)
	v_readfirstlane_b32 s3, v4
	v_sub_u32_e32 v4, 0, v3
	v_rcp_iflag_f32_e32 v5, v5
	v_add_u32_e32 v6, s3, v2
	v_mul_f32_e32 v5, 0x4f7ffffe, v5
	v_cvt_u32_f32_e32 v5, v5
	v_mul_lo_u32 v2, v4, v5
	v_mul_hi_u32 v2, v5, v2
	v_add_u32_e32 v2, v5, v2
	v_mul_hi_u32 v2, v6, v2
	v_mul_lo_u32 v4, v2, v3
	v_sub_u32_e32 v4, v6, v4
	v_add_u32_e32 v5, 1, v2
	v_cmp_ge_u32_e32 vcc, v4, v3
	s_nop 1
	v_cndmask_b32_e32 v2, v2, v5, vcc
	v_sub_u32_e32 v5, v4, v3
	v_cndmask_b32_e32 v4, v4, v5, vcc
	v_add_u32_e32 v5, 1, v2
	v_cmp_ge_u32_e32 vcc, v4, v3
	v_add_u32_e32 v4, 1, v6
	s_nop 0
	v_cndmask_b32_e32 v2, v2, v5, vcc
	v_mul_lo_u32 v5, v3, v2
	v_add_u32_e32 v3, v5, v3
	v_cmp_ne_u32_e32 vcc, v4, v3
	v_readfirstlane_b32 s98, v2
	s_and_saveexec_b64 s[8:9], vcc
	s_xor_b64 s[8:9], exec, s[8:9]
	s_cbranch_execz .LBB0_95
	s_waitcnt lgkmcnt(0)
	v_readfirstlane_b32 s99, v1
	s_add_u32 s98, s98, 1
	s_mul_i32 s98, s98, s99
	v_mov_b32_e32 v1, 0x3000
	s_mov_b32 s99, 0
.Lxb_nspin_0:
	global_load_dword v2, v1, s[60:61] offset:1024 sc1
	s_add_u32 s99, s99, 1
	s_waitcnt vmcnt(0)
	v_readfirstlane_b32 s100, v2
	s_sub_u32 s100, s100, s98
	s_cmp_ge_i32 s100, 0
	s_cbranch_scc1 .Lxb_ndone_0
	s_cmp_gt_u32 s99, 0x40000
	s_cbranch_scc1 .Lxb_ndone_0
	s_sleep 2
	s_branch .Lxb_nspin_0
.Lxb_ndone_0:
	s_waitcnt vmcnt(0)
	buffer_inv sc1
	s_waitcnt vmcnt(0)
.LBB0_95:
	s_andn2_saveexec_b64 s[8:9], s[8:9]
	s_cbranch_execz .LBB0_115
	s_mov_b64 s[8:9], exec
	buffer_wbl2 sc1
	s_waitcnt lgkmcnt(0)
	s_waitcnt vmcnt(0)
	v_mbcnt_lo_u32_b32 v2, s8, 0
	v_mbcnt_hi_u32_b32 v2, s9, v2
	v_cmp_eq_u32_e32 vcc, 0, v2
	s_and_saveexec_b64 s[10:11], vcc
	s_cbranch_execz .LBB0_98
	s_bcnt1_i32_b64 s3, s[8:9]
	v_mov_b32_e32 v3, 0x3000
	v_mov_b32_e32 v4, s3
	global_atomic_add v3, v3, v4, s[60:61] offset:1024 sc0
.LBB0_98:
	s_or_b64 exec, exec, s[10:11]
	v_cvt_f32_u32_e32 v4, v1
	s_waitcnt vmcnt(0)
	v_readfirstlane_b32 s3, v3
	s_add_u32 s10, s60, 0x3500
	s_addc_u32 s11, s61, 0
	v_rcp_iflag_f32_e32 v4, v4
	v_add_u32_e32 v2, s3, v2
	v_add_u32_e32 v5, 1, v2
	s_mov_b64 s[20:21], -1
	v_mul_f32_e32 v3, 0x4f7ffffe, v4
	v_cvt_u32_f32_e32 v3, v3
	v_sub_u32_e32 v4, 0, v1
	v_mul_lo_u32 v4, v4, v3
	v_mul_hi_u32 v4, v3, v4
	v_add_u32_e32 v3, v3, v4
	v_mul_hi_u32 v3, v2, v3
	v_mul_lo_u32 v4, v3, v1
	v_sub_u32_e32 v2, v2, v4
	v_add_u32_e32 v6, 1, v3
	v_cmp_ge_u32_e32 vcc, v2, v1
	v_sub_u32_e32 v4, v2, v1
	s_nop 0
	v_cndmask_b32_e32 v3, v3, v6, vcc
	v_cndmask_b32_e32 v2, v2, v4, vcc
	v_add_u32_e32 v4, 1, v3
	v_cmp_ge_u32_e32 vcc, v2, v1
	s_nop 1
	v_cndmask_b32_e32 v4, v3, v4, vcc
	v_mul_lo_u32 v2, v1, v4
	v_add_u32_e32 v1, v2, v1
	v_cmp_ne_u32_e32 vcc, v5, v1
	v_mov_b64_e32 v[2:3], s[10:11]
	v_readfirstlane_b32 s98, v1
	s_and_b64 vcc, exec, vcc
	s_cbranch_vccz .Lxb_ldone_0
	v_mov_b32_e32 v1, 0x3000
	s_mov_b32 s99, 0

.LBB0_224:
	s_or_b64 exec, exec, s[8:9]
	v_cvt_f32_u32_e32 v5, v3
	s_waitcnt vmcnt(0)
	v_readfirstlane_b32 s3, v4
	v_sub_u32_e32 v4, 0, v3
	v_rcp_iflag_f32_e32 v5, v5
	v_add_u32_e32 v6, s3, v2
	v_mul_f32_e32 v5, 0x4f7ffffe, v5
	v_cvt_u32_f32_e32 v5, v5
	v_mul_lo_u32 v2, v4, v5
	v_mul_hi_u32 v2, v5, v2
	v_add_u32_e32 v2, v5, v2
	v_mul_hi_u32 v2, v6, v2
	v_mul_lo_u32 v4, v2, v3
	v_sub_u32_e32 v4, v6, v4
	v_add_u32_e32 v5, 1, v2
	v_cmp_ge_u32_e32 vcc, v4, v3
	s_nop 1
	v_cndmask_b32_e32 v2, v2, v5, vcc
	v_sub_u32_e32 v5, v4, v3
	v_cndmask_b32_e32 v4, v4, v5, vcc
	v_add_u32_e32 v5, 1, v2
	v_cmp_ge_u32_e32 vcc, v4, v3
	v_add_u32_e32 v4, 1, v6
	s_nop 0
	v_cndmask_b32_e32 v2, v2, v5, vcc
	v_mul_lo_u32 v5, v3, v2
	v_add_u32_e32 v3, v5, v3
	v_cmp_ne_u32_e32 vcc, v4, v3
	v_readfirstlane_b32 s98, v2
	s_and_saveexec_b64 s[6:7], vcc
	s_xor_b64 s[6:7], exec, s[6:7]
	s_cbranch_execz .LBB0_238
	s_waitcnt lgkmcnt(0)
	v_readfirstlane_b32 s99, v1
	s_add_u32 s98, s98, 1
	s_mul_i32 s98, s98, s99
	v_mov_b32_e32 v1, 0x3000
	s_mov_b32 s99, 0

.Lxb_ndone_1:
	s_waitcnt vmcnt(0)
	buffer_inv sc1
	s_waitcnt vmcnt(0)
.LBB0_238:
	s_andn2_saveexec_b64 s[6:7], s[6:7]
	s_cbranch_execz .LBB0_258
	s_mov_b64 s[6:7], exec
	buffer_wbl2 sc1
	s_waitcnt lgkmcnt(0)
	s_waitcnt vmcnt(0)
	v_mbcnt_lo_u32_b32 v2, s6, 0
	v_mbcnt_hi_u32_b32 v2, s7, v2
	v_cmp_eq_u32_e32 vcc, 0, v2
	s_and_saveexec_b64 s[8:9], vcc
	s_cbranch_execz .LBB0_241
	s_bcnt1_i32_b64 s3, s[6:7]
	v_mov_b32_e32 v3, 0x3000
	v_mov_b32_e32 v4, s3
	global_atomic_add v3, v3, v4, s[60:61] offset:1024 sc0
.LBB0_241:
	s_or_b64 exec, exec, s[8:9]
	v_cvt_f32_u32_e32 v4, v1
	s_waitcnt vmcnt(0)
	v_readfirstlane_b32 s3, v3
	s_add_u32 s8, s60, 0x3500
	s_addc_u32 s9, s61, 0
	v_rcp_iflag_f32_e32 v4, v4
	v_add_u32_e32 v2, s3, v2
	v_add_u32_e32 v5, 1, v2
	s_mov_b64 s[10:11], -1
	v_mul_f32_e32 v3, 0x4f7ffffe, v4
	v_cvt_u32_f32_e32 v3, v3
	v_sub_u32_e32 v4, 0, v1
	v_mul_lo_u32 v4, v4, v3
	v_mul_hi_u32 v4, v3, v4
	v_add_u32_e32 v3, v3, v4
	v_mul_hi_u32 v3, v2, v3
	v_mul_lo_u32 v4, v3, v1
	v_sub_u32_e32 v2, v2, v4
	v_add_u32_e32 v6, 1, v3
	v_cmp_ge_u32_e32 vcc, v2, v1
	v_sub_u32_e32 v4, v2, v1
	s_nop 0
	v_cndmask_b32_e32 v3, v3, v6, vcc
	v_cndmask_b32_e32 v2, v2, v4, vcc
	v_add_u32_e32 v4, 1, v3
	v_cmp_ge_u32_e32 vcc, v2, v1
	s_nop 1
	v_cndmask_b32_e32 v4, v3, v4, vcc
	v_mul_lo_u32 v2, v1, v4
	v_add_u32_e32 v1, v2, v1
	v_cmp_ne_u32_e32 vcc, v5, v1
	v_mov_b64_e32 v[2:3], s[8:9]
	v_readfirstlane_b32 s98, v1
	s_and_b64 vcc, exec, vcc
	s_cbranch_vccz .Lxb_ldone_1
	v_mov_b32_e32 v1, 0x3000
	s_mov_b32 s99, 0

.Lxb_ndone_2:
	s_waitcnt vmcnt(0)
	buffer_inv sc1
	s_waitcnt vmcnt(0)
.LBB0_330:
	s_andn2_saveexec_b64 s[6:7], s[6:7]
	s_cbranch_execz .LBB0_350
	s_mov_b64 s[6:7], exec
	buffer_wbl2 sc1
	s_waitcnt lgkmcnt(0)
	s_waitcnt vmcnt(0)
	v_mbcnt_lo_u32_b32 v2, s6, 0
	v_mbcnt_hi_u32_b32 v2, s7, v2
	v_cmp_eq_u32_e32 vcc, 0, v2
	s_and_saveexec_b64 s[8:9], vcc
	s_cbranch_execz .LBB0_333
	s_bcnt1_i32_b64 s3, s[6:7]
	v_mov_b32_e32 v3, 0x3000
	v_mov_b32_e32 v4, s3
	global_atomic_add v3, v3, v4, s[60:61] offset:1024 sc0

.Lxb_ndone_3:
	s_waitcnt vmcnt(0)
	buffer_inv sc1
	s_waitcnt vmcnt(0)
.LBB0_426:
	s_andn2_saveexec_b64 s[6:7], s[6:7]
	s_cbranch_execz .LBB0_446
	s_mov_b64 s[6:7], exec
	buffer_wbl2 sc1
	s_waitcnt lgkmcnt(0)
	s_waitcnt vmcnt(0)
	v_mbcnt_lo_u32_b32 v2, s6, 0
	v_mbcnt_hi_u32_b32 v2, s7, v2
	v_cmp_eq_u32_e32 vcc, 0, v2
	s_and_saveexec_b64 s[8:9], vcc
	s_cbranch_execz .LBB0_429
	s_bcnt1_i32_b64 s3, s[6:7]
	v_mov_b32_e32 v3, 0x3000
	v_mov_b32_e32 v4, s3
	global_atomic_add v3, v3, v4, s[60:61] offset:1024 sc0

.Lxb_ndone_4:
	s_waitcnt vmcnt(0)
	buffer_inv sc1
	s_waitcnt vmcnt(0)
.LBB0_556:
	s_andn2_saveexec_b64 s[6:7], s[6:7]
	s_cbranch_execz .LBB0_576
	s_mov_b64 s[6:7], exec
	buffer_wbl2 sc1
	s_waitcnt lgkmcnt(0)
	s_waitcnt vmcnt(0)
	v_mbcnt_lo_u32_b32 v2, s6, 0
	v_mbcnt_hi_u32_b32 v2, s7, v2
	v_cmp_eq_u32_e32 vcc, 0, v2
	s_and_saveexec_b64 s[8:9], vcc
	s_cbranch_execz .LBB0_559
	s_bcnt1_i32_b64 s3, s[6:7]
	v_mov_b32_e32 v3, 0x3000
	v_mov_b32_e32 v4, s3
	global_atomic_add v3, v3, v4, s[60:61] offset:1024 sc0

.Lxb_ndone_5:
	s_waitcnt vmcnt(0)
	buffer_inv sc1
	s_waitcnt vmcnt(0)
.LBB0_706:
	s_andn2_saveexec_b64 s[6:7], s[6:7]
	s_cbranch_execz .LBB0_726
	s_mov_b64 s[6:7], exec
	buffer_wbl2 sc1
	s_waitcnt lgkmcnt(0)
	s_waitcnt vmcnt(0)
	v_mbcnt_lo_u32_b32 v2, s6, 0
	v_mbcnt_hi_u32_b32 v2, s7, v2
	v_cmp_eq_u32_e32 vcc, 0, v2
	s_and_saveexec_b64 s[8:9], vcc
	s_cbranch_execz .LBB0_709
	s_bcnt1_i32_b64 s3, s[6:7]
	v_mov_b32_e32 v3, 0x3000
	v_mov_b32_e32 v4, s3
	global_atomic_add v3, v3, v4, s[60:61] offset:1024 sc0

.Lxb_ndone_6:
	s_waitcnt vmcnt(0)
	buffer_inv sc1
	s_waitcnt vmcnt(0)
.LBB0_775:
	s_andn2_saveexec_b64 s[6:7], s[6:7]
	s_cbranch_execz .LBB0_795
	s_mov_b64 s[6:7], exec
	buffer_wbl2 sc1
	s_waitcnt lgkmcnt(0)
	s_waitcnt vmcnt(0)
	v_mbcnt_lo_u32_b32 v2, s6, 0
	v_mbcnt_hi_u32_b32 v2, s7, v2
	v_cmp_eq_u32_e32 vcc, 0, v2
	s_and_saveexec_b64 s[8:9], vcc
	s_cbranch_execz .LBB0_778
	s_bcnt1_i32_b64 s3, s[6:7]
	v_mov_b32_e32 v3, 0x3000
	v_mov_b32_e32 v4, s3
	global_atomic_add v3, v3, v4, s[60:61] offset:1024 sc0

.Lxb_ndone_7:
	s_waitcnt vmcnt(0)
	buffer_inv sc1
	s_waitcnt vmcnt(0)
.LBB0_868:
	s_andn2_saveexec_b64 s[6:7], s[6:7]
	s_cbranch_execz .LBB0_888
	s_mov_b64 s[6:7], exec
	buffer_wbl2 sc1
	s_waitcnt lgkmcnt(0)
	s_waitcnt vmcnt(0)
	v_mbcnt_lo_u32_b32 v2, s6, 0
	v_mbcnt_hi_u32_b32 v2, s7, v2
	v_cmp_eq_u32_e32 vcc, 0, v2
	s_and_saveexec_b64 s[8:9], vcc
	s_cbranch_execz .LBB0_871
	s_bcnt1_i32_b64 s3, s[6:7]
	v_mov_b32_e32 v3, 0x3000
	v_mov_b32_e32 v4, s3
	global_atomic_add v3, v3, v4, s[60:61] offset:1024 sc0

.Lxb_ndone_8:
	s_waitcnt vmcnt(0)
	buffer_inv sc1
	s_waitcnt vmcnt(0)
.LBB0_982:
	s_andn2_saveexec_b64 s[6:7], s[6:7]
	s_cbranch_execz .LBB0_1002
	s_mov_b64 s[6:7], exec
	buffer_wbl2 sc1
	s_waitcnt lgkmcnt(0)
	s_waitcnt vmcnt(0)
	v_mbcnt_lo_u32_b32 v2, s6, 0
	v_mbcnt_hi_u32_b32 v2, s7, v2
	v_cmp_eq_u32_e32 vcc, 0, v2
	s_and_saveexec_b64 s[8:9], vcc
	s_cbranch_execz .LBB0_985
	s_bcnt1_i32_b64 s3, s[6:7]
	v_mov_b32_e32 v3, 0x3000
	v_mov_b32_e32 v4, s3
	global_atomic_add v3, v3, v4, s[60:61] offset:1024 sc0

.Lxb_ndone_9:
	s_waitcnt vmcnt(0)
	buffer_inv sc1
	s_waitcnt vmcnt(0)
.LBB0_1057:
	s_andn2_saveexec_b64 s[6:7], s[6:7]
	s_cbranch_execz .LBB0_1077
	s_mov_b64 s[6:7], exec
	buffer_wbl2 sc1
	s_waitcnt lgkmcnt(0)
	s_waitcnt vmcnt(0)
	v_mbcnt_lo_u32_b32 v2, s6, 0
	v_mbcnt_hi_u32_b32 v2, s7, v2
	v_cmp_eq_u32_e32 vcc, 0, v2
	s_and_saveexec_b64 s[8:9], vcc
	s_cbranch_execz .LBB0_1060
	s_bcnt1_i32_b64 s3, s[6:7]
	v_mov_b32_e32 v3, 0x3000
	v_mov_b32_e32 v4, s3
	global_atomic_add v3, v3, v4, s[60:61] offset:1024 sc0

.Lxb_ndone_10:
	s_waitcnt vmcnt(0)
	buffer_inv sc1
	s_waitcnt vmcnt(0)
.LBB0_1141:
	s_andn2_saveexec_b64 s[6:7], s[6:7]
	s_cbranch_execz .LBB0_1161
	s_mov_b64 s[6:7], exec
	buffer_wbl2 sc1
	s_waitcnt lgkmcnt(0)
	s_waitcnt vmcnt(0)
	v_mbcnt_lo_u32_b32 v2, s6, 0
	v_mbcnt_hi_u32_b32 v2, s7, v2
	v_cmp_eq_u32_e32 vcc, 0, v2
	s_and_saveexec_b64 s[8:9], vcc
	s_cbranch_execz .LBB0_1144
	s_bcnt1_i32_b64 s3, s[6:7]
	v_mov_b32_e32 v3, 0x3000
	v_mov_b32_e32 v4, s3
	global_atomic_add v3, v3, v4, s[60:61] offset:1024 sc0

.LBB0_1277:
	s_or_b64 exec, exec, s[6:7]
	v_cvt_f32_u32_e32 v5, v3
	s_waitcnt vmcnt(0)
	v_readfirstlane_b32 s4, v4
	v_sub_u32_e32 v4, 0, v3
	v_rcp_iflag_f32_e32 v5, v5
	v_add_u32_e32 v6, s4, v2
	v_mul_f32_e32 v5, 0x4f7ffffe, v5
	v_cvt_u32_f32_e32 v5, v5
	v_mul_lo_u32 v2, v4, v5
	v_mul_hi_u32 v2, v5, v2
	v_add_u32_e32 v2, v5, v2
	v_mul_hi_u32 v2, v6, v2
	v_mul_lo_u32 v4, v2, v3
	v_sub_u32_e32 v4, v6, v4
	v_add_u32_e32 v5, 1, v2
	v_cmp_ge_u32_e32 vcc, v4, v3
	s_nop 1
	v_cndmask_b32_e32 v2, v2, v5, vcc
	v_sub_u32_e32 v5, v4, v3
	v_cndmask_b32_e32 v4, v4, v5, vcc
	v_add_u32_e32 v5, 1, v2
	v_cmp_ge_u32_e32 vcc, v4, v3
	v_add_u32_e32 v4, 1, v6
	s_nop 0
	v_cndmask_b32_e32 v2, v2, v5, vcc
	v_mul_lo_u32 v5, v3, v2
	v_add_u32_e32 v3, v5, v3
	v_cmp_ne_u32_e32 vcc, v4, v3
	v_readfirstlane_b32 s98, v2
	s_and_saveexec_b64 s[4:5], vcc
	s_xor_b64 s[4:5], exec, s[4:5]
	s_cbranch_execz .LBB0_1291
	s_waitcnt lgkmcnt(0)
	v_readfirstlane_b32 s99, v1
	s_add_u32 s98, s98, 1
	s_mul_i32 s98, s98, s99
	v_mov_b32_e32 v1, 0x3000
	s_mov_b32 s99, 0

.Lxb_ndone_11:
	s_waitcnt vmcnt(0)
	buffer_inv sc1
	s_waitcnt vmcnt(0)
.LBB0_1291:
	s_andn2_saveexec_b64 s[4:5], s[4:5]
	s_cbranch_execz .LBB0_1311
	s_mov_b64 s[4:5], exec
	buffer_wbl2 sc1
	s_waitcnt lgkmcnt(0)
	s_waitcnt vmcnt(0)
	v_mbcnt_lo_u32_b32 v2, s4, 0
	v_mbcnt_hi_u32_b32 v2, s5, v2
	v_cmp_eq_u32_e32 vcc, 0, v2
	s_and_saveexec_b64 s[6:7], vcc
	s_cbranch_execz .LBB0_1294
	s_bcnt1_i32_b64 s4, s[4:5]
	v_mov_b32_e32 v3, 0x3000
	v_mov_b32_e32 v4, s4
	global_atomic_add v3, v3, v4, s[60:61] offset:1024 sc0
.LBB0_1294:
	s_or_b64 exec, exec, s[6:7]
	v_cvt_f32_u32_e32 v4, v1
	s_waitcnt vmcnt(0)
	v_readfirstlane_b32 s4, v3
	s_add_u32 s6, s60, 0x3500
	s_addc_u32 s7, s61, 0
	v_rcp_iflag_f32_e32 v4, v4
	v_add_u32_e32 v2, s4, v2
	v_add_u32_e32 v5, 1, v2
	s_mov_b64 s[8:9], -1
	v_mul_f32_e32 v3, 0x4f7ffffe, v4
	v_cvt_u32_f32_e32 v3, v3
	v_sub_u32_e32 v4, 0, v1
	v_mul_lo_u32 v4, v4, v3
	v_mul_hi_u32 v4, v3, v4
	v_add_u32_e32 v3, v3, v4
	v_mul_hi_u32 v3, v2, v3
	v_mul_lo_u32 v4, v3, v1
	v_sub_u32_e32 v2, v2, v4
	v_add_u32_e32 v6, 1, v3
	v_cmp_ge_u32_e32 vcc, v2, v1
	v_sub_u32_e32 v4, v2, v1
	s_nop 0
	v_cndmask_b32_e32 v3, v3, v6, vcc
	v_cndmask_b32_e32 v2, v2, v4, vcc
	v_add_u32_e32 v4, 1, v3
	v_cmp_ge_u32_e32 vcc, v2, v1
	s_nop 1
	v_cndmask_b32_e32 v4, v3, v4, vcc
	v_mul_lo_u32 v2, v1, v4
	v_add_u32_e32 v1, v2, v1
	v_cmp_ne_u32_e32 vcc, v5, v1
	v_mov_b64_e32 v[2:3], s[6:7]
	v_readfirstlane_b32 s98, v1
	s_and_b64 vcc, exec, vcc
	s_cbranch_vccz .Lxb_ldone_11
	v_mov_b32_e32 v1, 0x3000
	s_mov_b32 s99, 0

.Lxb_ndone_12:
	s_waitcnt vmcnt(0)
	buffer_inv sc1
	s_waitcnt vmcnt(0)
.LBB0_1394:
	s_andn2_saveexec_b64 s[4:5], s[4:5]
	s_cbranch_execz .LBB0_1414
	s_mov_b64 s[4:5], exec
	buffer_wbl2 sc1
	s_waitcnt lgkmcnt(0)
	s_waitcnt vmcnt(0)
	v_mbcnt_lo_u32_b32 v2, s4, 0
	v_mbcnt_hi_u32_b32 v2, s5, v2
	v_cmp_eq_u32_e32 vcc, 0, v2
	s_and_saveexec_b64 s[6:7], vcc
	s_cbranch_execz .LBB0_1397
	s_bcnt1_i32_b64 s4, s[4:5]
	v_mov_b32_e32 v3, 0x3000
	v_mov_b32_e32 v4, s4
	global_atomic_add v3, v3, v4, s[60:61] offset:1024 sc0

.Lxb_ndone_13:
	s_waitcnt vmcnt(0)
	buffer_inv sc1
	s_waitcnt vmcnt(0)
.LBB0_1497:
	s_andn2_saveexec_b64 s[4:5], s[4:5]
	s_cbranch_execz .LBB0_1517
	s_mov_b64 s[4:5], exec
	buffer_wbl2 sc1
	s_waitcnt lgkmcnt(0)
	s_waitcnt vmcnt(0)
	v_mbcnt_lo_u32_b32 v2, s4, 0
	v_mbcnt_hi_u32_b32 v2, s5, v2
	v_cmp_eq_u32_e32 vcc, 0, v2
	s_and_saveexec_b64 s[6:7], vcc
	s_cbranch_execz .LBB0_1500
	s_bcnt1_i32_b64 s4, s[4:5]
	v_mov_b32_e32 v3, 0x3000
	v_mov_b32_e32 v4, s4
	global_atomic_add v3, v3, v4, s[60:61] offset:1024 sc0
